# ln1_router logits loop software-pipelined (8-deep ring of weight/LDS operand registers, counted waits) on top of MoE rowmap/wait changes
# speedup vs baseline: 1.0071x; 1.0071x over previous
.LBB0_1388:
	v_add_co_u32_e32 v8, vcc, 0x55664000, v48
	s_nop 1
	v_addc_co_u32_e32 v9, vcc, 0, v49, vcc
	v_add_co_u32_e32 v6, vcc, 0x55674000, v48
	s_nop 1
	v_addc_co_u32_e32 v7, vcc, 0, v49, vcc
	ds_read_b128 v[120:123], v10 offset:0
	global_load_dwordx4 v[56:59], v[8:9], off offset:2048
	global_load_dwordx4 v[88:91], v[6:7], off offset:2048
	ds_read_b128 v[124:127], v10 offset:64
	global_load_dwordx4 v[60:63], v[8:9], off offset:2112
	global_load_dwordx4 v[92:95], v[6:7], off offset:2112
	ds_read_b128 v[128:131], v10 offset:128
	global_load_dwordx4 v[64:67], v[8:9], off offset:2176
	global_load_dwordx4 v[96:99], v[6:7], off offset:2176
	ds_read_b128 v[132:135], v10 offset:192
	global_load_dwordx4 v[68:71], v[8:9], off offset:2240
	global_load_dwordx4 v[100:103], v[6:7], off offset:2240
	ds_read_b128 v[136:139], v10 offset:256
	global_load_dwordx4 v[72:75], v[8:9], off offset:2304
	global_load_dwordx4 v[104:107], v[6:7], off offset:2304
	ds_read_b128 v[140:143], v10 offset:320
	global_load_dwordx4 v[76:79], v[8:9], off offset:2368
	global_load_dwordx4 v[108:111], v[6:7], off offset:2368
	ds_read_b128 v[144:147], v10 offset:384
	global_load_dwordx4 v[80:83], v[8:9], off offset:2432
	global_load_dwordx4 v[112:115], v[6:7], off offset:2432
	ds_read_b128 v[148:151], v10 offset:448
	global_load_dwordx4 v[84:87], v[8:9], off offset:2496
	global_load_dwordx4 v[116:119], v[6:7], off offset:2496
	s_waitcnt vmcnt(15) lgkmcnt(7)
	v_mfma_f32_16x16x32_bf16 v[2:5], v[120:123], v[56:59], v[2:5]
	s_waitcnt vmcnt(14)
	v_mfma_f32_16x16x32_bf16 v[2:5], v[120:123], v[88:91], v[2:5]
	ds_read_b128 v[120:123], v10 offset:512
	global_load_dwordx4 v[56:59], v[8:9], off offset:2560
	global_load_dwordx4 v[88:91], v[6:7], off offset:2560
	s_waitcnt vmcnt(15) lgkmcnt(7)
	v_mfma_f32_16x16x32_bf16 v[2:5], v[124:127], v[60:63], v[2:5]
	s_waitcnt vmcnt(14)
	v_mfma_f32_16x16x32_bf16 v[2:5], v[124:127], v[92:95], v[2:5]
	ds_read_b128 v[124:127], v10 offset:576
	global_load_dwordx4 v[60:63], v[8:9], off offset:2624
	global_load_dwordx4 v[92:95], v[6:7], off offset:2624
	s_waitcnt vmcnt(15) lgkmcnt(7)
	v_mfma_f32_16x16x32_bf16 v[2:5], v[128:131], v[64:67], v[2:5]
	s_waitcnt vmcnt(14)
	v_mfma_f32_16x16x32_bf16 v[2:5], v[128:131], v[96:99], v[2:5]
	ds_read_b128 v[128:131], v10 offset:640
	global_load_dwordx4 v[64:67], v[8:9], off offset:2688
	global_load_dwordx4 v[96:99], v[6:7], off offset:2688
	s_waitcnt vmcnt(15) lgkmcnt(7)
	v_mfma_f32_16x16x32_bf16 v[2:5], v[132:135], v[68:71], v[2:5]
	s_waitcnt vmcnt(14)
	v_mfma_f32_16x16x32_bf16 v[2:5], v[132:135], v[100:103], v[2:5]
	ds_read_b128 v[132:135], v10 offset:704
	global_load_dwordx4 v[68:71], v[8:9], off offset:2752
	global_load_dwordx4 v[100:103], v[6:7], off offset:2752
	s_waitcnt vmcnt(15) lgkmcnt(7)
	v_mfma_f32_16x16x32_bf16 v[2:5], v[136:139], v[72:75], v[2:5]
	s_waitcnt vmcnt(14)
	v_mfma_f32_16x16x32_bf16 v[2:5], v[136:139], v[104:107], v[2:5]
	ds_read_b128 v[136:139], v10 offset:768
	global_load_dwordx4 v[72:75], v[8:9], off offset:2816
	global_load_dwordx4 v[104:107], v[6:7], off offset:2816
	s_waitcnt vmcnt(15) lgkmcnt(7)
	v_mfma_f32_16x16x32_bf16 v[2:5], v[140:143], v[76:79], v[2:5]
	s_waitcnt vmcnt(14)
	v_mfma_f32_16x16x32_bf16 v[2:5], v[140:143], v[108:111], v[2:5]
	ds_read_b128 v[140:143], v10 offset:832
	global_load_dwordx4 v[76:79], v[8:9], off offset:2880
	global_load_dwordx4 v[108:111], v[6:7], off offset:2880
	s_waitcnt vmcnt(15) lgkmcnt(7)
	v_mfma_f32_16x16x32_bf16 v[2:5], v[144:147], v[80:83], v[2:5]
	s_waitcnt vmcnt(14)
	v_mfma_f32_16x16x32_bf16 v[2:5], v[144:147], v[112:115], v[2:5]
	ds_read_b128 v[144:147], v10 offset:896
	global_load_dwordx4 v[80:83], v[8:9], off offset:2944
	global_load_dwordx4 v[112:115], v[6:7], off offset:2944
	s_waitcnt vmcnt(15) lgkmcnt(7)
	v_mfma_f32_16x16x32_bf16 v[2:5], v[148:151], v[84:87], v[2:5]
	s_waitcnt vmcnt(14)
	v_mfma_f32_16x16x32_bf16 v[2:5], v[148:151], v[116:119], v[2:5]
	ds_read_b128 v[148:151], v10 offset:960
	global_load_dwordx4 v[84:87], v[8:9], off offset:3008
	global_load_dwordx4 v[116:119], v[6:7], off offset:3008
	s_waitcnt vmcnt(15) lgkmcnt(7)
	v_mfma_f32_16x16x32_bf16 v[2:5], v[120:123], v[56:59], v[2:5]
	s_waitcnt vmcnt(14)
	v_mfma_f32_16x16x32_bf16 v[2:5], v[120:123], v[88:91], v[2:5]
	ds_read_b128 v[120:123], v10 offset:1024
	global_load_dwordx4 v[56:59], v[8:9], off offset:3072
	global_load_dwordx4 v[88:91], v[6:7], off offset:3072
	s_waitcnt vmcnt(15) lgkmcnt(7)
	v_mfma_f32_16x16x32_bf16 v[2:5], v[124:127], v[60:63], v[2:5]
	s_waitcnt vmcnt(14)
	v_mfma_f32_16x16x32_bf16 v[2:5], v[124:127], v[92:95], v[2:5]
	ds_read_b128 v[124:127], v10 offset:1088
	global_load_dwordx4 v[60:63], v[8:9], off offset:3136
	global_load_dwordx4 v[92:95], v[6:7], off offset:3136
	s_waitcnt vmcnt(15) lgkmcnt(7)
	v_mfma_f32_16x16x32_bf16 v[2:5], v[128:131], v[64:67], v[2:5]
	s_waitcnt vmcnt(14)
	v_mfma_f32_16x16x32_bf16 v[2:5], v[128:131], v[96:99], v[2:5]
	ds_read_b128 v[128:131], v10 offset:1152
	global_load_dwordx4 v[64:67], v[8:9], off offset:3200
	global_load_dwordx4 v[96:99], v[6:7], off offset:3200
	s_waitcnt vmcnt(15) lgkmcnt(7)
	v_mfma_f32_16x16x32_bf16 v[2:5], v[132:135], v[68:71], v[2:5]
	s_waitcnt vmcnt(14)
	v_mfma_f32_16x16x32_bf16 v[2:5], v[132:135], v[100:103], v[2:5]
	ds_read_b128 v[132:135], v10 offset:1216
	global_load_dwordx4 v[68:71], v[8:9], off offset:3264
	global_load_dwordx4 v[100:103], v[6:7], off offset:3264
	s_waitcnt vmcnt(15) lgkmcnt(7)
	v_mfma_f32_16x16x32_bf16 v[2:5], v[136:139], v[72:75], v[2:5]
	s_waitcnt vmcnt(14)
	v_mfma_f32_16x16x32_bf16 v[2:5], v[136:139], v[104:107], v[2:5]
	ds_read_b128 v[136:139], v10 offset:1280
	global_load_dwordx4 v[72:75], v[8:9], off offset:3328
	global_load_dwordx4 v[104:107], v[6:7], off offset:3328
	s_waitcnt vmcnt(15) lgkmcnt(7)
	v_mfma_f32_16x16x32_bf16 v[2:5], v[140:143], v[76:79], v[2:5]
	s_waitcnt vmcnt(14)
	v_mfma_f32_16x16x32_bf16 v[2:5], v[140:143], v[108:111], v[2:5]
	ds_read_b128 v[140:143], v10 offset:1344
	global_load_dwordx4 v[76:79], v[8:9], off offset:3392
	global_load_dwordx4 v[108:111], v[6:7], off offset:3392
	s_waitcnt vmcnt(15) lgkmcnt(7)
	v_mfma_f32_16x16x32_bf16 v[2:5], v[144:147], v[80:83], v[2:5]
	s_waitcnt vmcnt(14)
	v_mfma_f32_16x16x32_bf16 v[2:5], v[144:147], v[112:115], v[2:5]
	ds_read_b128 v[144:147], v10 offset:1408
	global_load_dwordx4 v[80:83], v[8:9], off offset:3456
	global_load_dwordx4 v[112:115], v[6:7], off offset:3456
	s_waitcnt vmcnt(15) lgkmcnt(7)
	v_mfma_f32_16x16x32_bf16 v[2:5], v[148:151], v[84:87], v[2:5]
	s_waitcnt vmcnt(14)
	v_mfma_f32_16x16x32_bf16 v[2:5], v[148:151], v[116:119], v[2:5]
	ds_read_b128 v[148:151], v10 offset:1472
	global_load_dwordx4 v[84:87], v[8:9], off offset:3520
	global_load_dwordx4 v[116:119], v[6:7], off offset:3520
	s_waitcnt vmcnt(15) lgkmcnt(7)
	v_mfma_f32_16x16x32_bf16 v[2:5], v[120:123], v[56:59], v[2:5]
	s_waitcnt vmcnt(14)
	v_mfma_f32_16x16x32_bf16 v[2:5], v[120:123], v[88:91], v[2:5]
	ds_read_b128 v[120:123], v10 offset:1536
	global_load_dwordx4 v[56:59], v[8:9], off offset:3584
	global_load_dwordx4 v[88:91], v[6:7], off offset:3584
	s_waitcnt vmcnt(15) lgkmcnt(7)
	v_mfma_f32_16x16x32_bf16 v[2:5], v[124:127], v[60:63], v[2:5]
	s_waitcnt vmcnt(14)
	v_mfma_f32_16x16x32_bf16 v[2:5], v[124:127], v[92:95], v[2:5]
	ds_read_b128 v[124:127], v10 offset:1600
	global_load_dwordx4 v[60:63], v[8:9], off offset:3648
	global_load_dwordx4 v[92:95], v[6:7], off offset:3648
	s_waitcnt vmcnt(15) lgkmcnt(7)
	v_mfma_f32_16x16x32_bf16 v[2:5], v[128:131], v[64:67], v[2:5]
	s_waitcnt vmcnt(14)
	v_mfma_f32_16x16x32_bf16 v[2:5], v[128:131], v[96:99], v[2:5]
	ds_read_b128 v[128:131], v10 offset:1664
	global_load_dwordx4 v[64:67], v[8:9], off offset:3712
	global_load_dwordx4 v[96:99], v[6:7], off offset:3712
	s_waitcnt vmcnt(15) lgkmcnt(7)
	v_mfma_f32_16x16x32_bf16 v[2:5], v[132:135], v[68:71], v[2:5]
	s_waitcnt vmcnt(14)
	v_mfma_f32_16x16x32_bf16 v[2:5], v[132:135], v[100:103], v[2:5]
	ds_read_b128 v[132:135], v10 offset:1728
	global_load_dwordx4 v[68:71], v[8:9], off offset:3776
	global_load_dwordx4 v[100:103], v[6:7], off offset:3776
	s_waitcnt vmcnt(15) lgkmcnt(7)
	v_mfma_f32_16x16x32_bf16 v[2:5], v[136:139], v[72:75], v[2:5]
	s_waitcnt vmcnt(14)
	v_mfma_f32_16x16x32_bf16 v[2:5], v[136:139], v[104:107], v[2:5]
	ds_read_b128 v[136:139], v10 offset:1792
	global_load_dwordx4 v[72:75], v[8:9], off offset:3840
	global_load_dwordx4 v[104:107], v[6:7], off offset:3840
	s_waitcnt vmcnt(15) lgkmcnt(7)
	v_mfma_f32_16x16x32_bf16 v[2:5], v[140:143], v[76:79], v[2:5]
	s_waitcnt vmcnt(14)
	v_mfma_f32_16x16x32_bf16 v[2:5], v[140:143], v[108:111], v[2:5]
	ds_read_b128 v[140:143], v10 offset:1856
	global_load_dwordx4 v[76:79], v[8:9], off offset:3904
	global_load_dwordx4 v[108:111], v[6:7], off offset:3904
	s_waitcnt vmcnt(15) lgkmcnt(7)
	v_mfma_f32_16x16x32_bf16 v[2:5], v[144:147], v[80:83], v[2:5]
	s_waitcnt vmcnt(14)
	v_mfma_f32_16x16x32_bf16 v[2:5], v[144:147], v[112:115], v[2:5]
	ds_read_b128 v[144:147], v10 offset:1920
	global_load_dwordx4 v[80:83], v[8:9], off offset:3968
	global_load_dwordx4 v[112:115], v[6:7], off offset:3968
	s_waitcnt vmcnt(15) lgkmcnt(7)
	v_mfma_f32_16x16x32_bf16 v[2:5], v[148:151], v[84:87], v[2:5]
	s_waitcnt vmcnt(14)
	v_mfma_f32_16x16x32_bf16 v[2:5], v[148:151], v[116:119], v[2:5]
	ds_read_b128 v[148:151], v10 offset:1984
	global_load_dwordx4 v[84:87], v[8:9], off offset:4032
	global_load_dwordx4 v[116:119], v[6:7], off offset:4032
	s_waitcnt vmcnt(15) lgkmcnt(7)
	v_mfma_f32_16x16x32_bf16 v[2:5], v[120:123], v[56:59], v[2:5]
	s_waitcnt vmcnt(14)
	v_mfma_f32_16x16x32_bf16 v[2:5], v[120:123], v[88:91], v[2:5]
	s_waitcnt vmcnt(13) lgkmcnt(6)
	v_mfma_f32_16x16x32_bf16 v[2:5], v[124:127], v[60:63], v[2:5]
	s_waitcnt vmcnt(12)
	v_mfma_f32_16x16x32_bf16 v[2:5], v[124:127], v[92:95], v[2:5]
	s_waitcnt vmcnt(11) lgkmcnt(5)
	v_mfma_f32_16x16x32_bf16 v[2:5], v[128:131], v[64:67], v[2:5]
	s_waitcnt vmcnt(10)
	v_mfma_f32_16x16x32_bf16 v[2:5], v[128:131], v[96:99], v[2:5]
	s_waitcnt vmcnt(9) lgkmcnt(4)
	v_mfma_f32_16x16x32_bf16 v[2:5], v[132:135], v[68:71], v[2:5]
	s_waitcnt vmcnt(8)
	v_mfma_f32_16x16x32_bf16 v[2:5], v[132:135], v[100:103], v[2:5]
	s_waitcnt vmcnt(7) lgkmcnt(3)
	v_mfma_f32_16x16x32_bf16 v[2:5], v[136:139], v[72:75], v[2:5]
	s_waitcnt vmcnt(6)
	v_mfma_f32_16x16x32_bf16 v[2:5], v[136:139], v[104:107], v[2:5]
	s_waitcnt vmcnt(5) lgkmcnt(2)
	v_mfma_f32_16x16x32_bf16 v[2:5], v[140:143], v[76:79], v[2:5]
	s_waitcnt vmcnt(4)
	v_mfma_f32_16x16x32_bf16 v[2:5], v[140:143], v[108:111], v[2:5]
	s_waitcnt vmcnt(3) lgkmcnt(1)
	v_mfma_f32_16x16x32_bf16 v[2:5], v[144:147], v[80:83], v[2:5]
	s_waitcnt vmcnt(2)
	v_mfma_f32_16x16x32_bf16 v[2:5], v[144:147], v[112:115], v[2:5]
	s_waitcnt vmcnt(1) lgkmcnt(0)
	v_mfma_f32_16x16x32_bf16 v[2:5], v[148:151], v[84:87], v[2:5]
	s_waitcnt vmcnt(0)
	v_mfma_f32_16x16x32_bf16 v[2:5], v[148:151], v[116:119], v[2:5]
	s_nop 0
	global_load_dword v6, v[38:39], off
	s_waitcnt vmcnt(0)
	s_nop 4
	v_add_f32_e32 v2, v2, v6
	v_add_f32_e32 v3, v3, v6
	v_add_f32_e32 v4, v4, v6
	v_add_f32_e32 v5, v5, v6
	ds_write2_b32 v196, v2, v3 offset1:33
	ds_write2_b32 v196, v4, v5 offset0:66 offset1:99
	s_waitcnt lgkmcnt(0)
	s_barrier
	s_and_saveexec_b64 s[0:1], s[14:15]
	s_cbranch_execz .LBB0_1765
	ds_read2_b32 v[6:7], v192 offset1:1
	s_mov_b32 s2, 0xff800000
	v_mov_b32_e32 v3, 0xff800000
	v_mov_b32_e32 v8, 0xff800000
	v_mov_b32_e32 v2, 0
	s_waitcnt lgkmcnt(0)
	v_cmp_lg_f32_e32 vcc, s2, v6
	v_mov_b32_e32 v4, 0
	v_mov_b32_e32 v5, 0
	v_cndmask_b32_e32 v6, v3, v6, vcc
	v_cmp_lt_f32_e32 vcc, s2, v7
	v_mov_b32_e32 v3, 0
	v_mov_b32_e32 v10, 0xff800000
	v_mov_b32_e32 v9, 0xff800000
	s_and_saveexec_b64 s[2:3], vcc
	s_cbranch_execz .LBB0_1404
	v_cmp_ngt_f32_e32 vcc, v7, v6
	s_and_saveexec_b64 s[4:5], vcc
	s_xor_b64 s[10:11], exec, s[4:5]
	s_cbranch_execz .LBB0_1401
	v_cmp_ngt_f32_e32 vcc, v7, v8
	s_and_saveexec_b64 s[4:5], vcc
	s_xor_b64 s[18:19], exec, s[4:5]
	s_cbranch_execz .LBB0_1398
	v_cmp_ngt_f32_e32 vcc, v7, v8
	s_and_saveexec_b64 s[4:5], vcc
	s_xor_b64 s[20:21], exec, s[4:5]
	v_mov_b32_e32 v8, 0xff800000
	v_mov_b32_e32 v10, 0xff800000
	s_or_saveexec_b64 s[20:21], s[20:21]
	v_mov_b32_e32 v4, 0
	v_mov_b32_e32 v5, 1
	v_mov_b32_e32 v9, v7
	s_xor_b64 exec, exec, s[20:21]
	v_mov_b32_e32 v8, 0xff800000
	v_mov_b32_e32 v9, 0xff800000
	v_mov_b32_e32 v5, 0
	v_mov_b32_e32 v10, v7
	v_mov_b32_e32 v4, 1
	s_or_b64 exec, exec, s[20:21]
